# code placement test: P2 loop head at mod-8 phase 0 (pad before it) and a second unexecuted 4-byte pad after the P2 loop so the fp8 loop heads stay at phase 0
# speedup vs baseline: 1.0073x; 1.0064x over previous
.LBB0_355:
	s_ashr_i32 s4, s93, 31
	s_lshr_b32 s4, s4, 26
	s_add_i32 s4, s93, s4
	s_and_b32 s4, s4, 0xffffc0
	s_sub_i32 s4, s93, s4
	s_lshl_b32 s4, s4, 8
	s_add_i32 s4, s4, s74
	s_nop 15
	s_nop 15
	v_mbcnt_lo_u32_b32 v137, -1, 0
	v_mbcnt_hi_u32_b32 v137, -1, v137
	s_nop 0
	v_and_or_b32 v128, v137, 15, s4
	v_ashrrev_i32_e32 v129, 31, v128
	v_or_b32_e32 v132, 16, v128
	v_lshl_add_u64 v[130:131], v[128:129], 2, s[42:43]
	v_ashrrev_i32_e32 v133, 31, v132
	v_or_b32_e32 v138, 32, v128
	global_load_dword v136, v[130:131], off
	v_lshl_add_u64 v[134:135], v[132:133], 2, s[42:43]
	v_ashrrev_i32_e32 v139, 31, v138
	v_or_b32_e32 v152, 48, v128
	global_load_dword v144, v[134:135], off
	v_lshl_add_u64 v[134:135], v[138:139], 2, s[42:43]
	v_ashrrev_i32_e32 v153, 31, v152
	global_load_dword v146, v[134:135], off
	v_lshl_add_u64 v[134:135], v[152:153], 2, s[42:43]
	global_load_dword v134, v[134:135], off
	s_lshl_b32 s4, s92, 8
	v_and_b32_e32 v135, -16, v137
	s_or_b32 s4, s4, s84
	v_add_u32_e32 v140, s4, v135
	v_ashrrev_i32_e32 v141, 31, v140
	v_lshl_add_u64 v[154:155], v[140:141], 1, s[40:41]
	v_lshlrev_b64 v[140:141], 13, v[132:133]
	global_load_dword v156, v[130:131], off offset:512
	global_load_dword v158, v[130:131], off offset:576
	global_load_dword v132, v[130:131], off offset:640
	s_nop 0
	global_load_dword v130, v[130:131], off offset:704
	v_lshlrev_b64 v[138:139], 13, v[138:139]
	v_lshlrev_b64 v[128:129], 13, v[128:129]
	v_lshl_add_u64 v[160:161], v[154:155], 0, v[140:141]
	v_lshl_add_u64 v[162:163], v[154:155], 0, v[138:139]
	v_lshl_add_u64 v[128:129], v[154:155], 0, v[128:129]
	s_mov_b64 s[4:5], 0x100000
	s_waitcnt vmcnt(7)
	v_pk_mul_f32 v[138:139], v[126:127], v[136:137] op_sel_hi:[1,0]
	v_pk_mul_f32 v[140:141], v[124:125], v[136:137] op_sel_hi:[1,0]
	v_pk_mul_f32 v[142:143], v[122:123], v[136:137] op_sel_hi:[1,0]
	v_pk_mul_f32 v[148:149], v[120:121], v[136:137] op_sel_hi:[1,0]
	v_pk_mul_f32 v[150:151], v[94:95], v[136:137] op_sel_hi:[1,0]
	v_pk_mul_f32 v[164:165], v[92:93], v[136:137] op_sel_hi:[1,0]
	v_pk_mul_f32 v[166:167], v[90:91], v[136:137] op_sel_hi:[1,0]
	v_pk_mul_f32 v[168:169], v[88:89], v[136:137] op_sel_hi:[1,0]
	v_cvt_pk_bf16_f32 v136, v140, v141
	v_cvt_pk_bf16_f32 v137, v138, v139
	v_cvt_pk_bf16_f32 v138, v148, v149
	v_cvt_pk_bf16_f32 v139, v142, v143
	v_cvt_pk_bf16_f32 v140, v164, v165
	v_cvt_pk_bf16_f32 v141, v150, v151
	s_nop 0
	v_cvt_pk_bf16_f32 v142, v168, v169
	v_cvt_pk_bf16_f32 v143, v166, v167
	s_waitcnt vmcnt(6)
	v_pk_mul_f32 v[148:149], v[118:119], v[144:145] op_sel_hi:[1,0]
	v_pk_mul_f32 v[150:151], v[116:117], v[144:145] op_sel_hi:[1,0]
	v_pk_mul_f32 v[164:165], v[114:115], v[144:145] op_sel_hi:[1,0]
	v_pk_mul_f32 v[166:167], v[112:113], v[144:145] op_sel_hi:[1,0]
	v_pk_mul_f32 v[168:169], v[86:87], v[144:145] op_sel_hi:[1,0]
	v_pk_mul_f32 v[170:171], v[84:85], v[144:145] op_sel_hi:[1,0]
	v_pk_mul_f32 v[172:173], v[82:83], v[144:145] op_sel_hi:[1,0]
	v_pk_mul_f32 v[144:145], v[80:81], v[144:145] op_sel_hi:[1,0]
	global_store_dwordx4 v[128:129], v[136:139], off
	global_store_dwordx4 v[128:129], v[140:143], off offset:16
	s_waitcnt vmcnt(7)
	v_pk_mul_f32 v[174:175], v[110:111], v[146:147] op_sel_hi:[1,0]
	v_cvt_pk_bf16_f32 v136, v150, v151
	v_cvt_pk_bf16_f32 v137, v148, v149
	v_cvt_pk_bf16_f32 v138, v166, v167
	v_cvt_pk_bf16_f32 v139, v164, v165
	v_cvt_pk_bf16_f32 v140, v170, v171
	v_cvt_pk_bf16_f32 v141, v168, v169
	v_pk_mul_f32 v[176:177], v[108:109], v[146:147] op_sel_hi:[1,0]
	v_pk_mul_f32 v[178:179], v[106:107], v[146:147] op_sel_hi:[1,0]
	v_pk_mul_f32 v[180:181], v[104:105], v[146:147] op_sel_hi:[1,0]
	v_pk_mul_f32 v[182:183], v[78:79], v[146:147] op_sel_hi:[1,0]
	v_pk_mul_f32 v[184:185], v[76:77], v[146:147] op_sel_hi:[1,0]
	v_pk_mul_f32 v[186:187], v[74:75], v[146:147] op_sel_hi:[1,0]
	v_pk_mul_f32 v[188:189], v[72:73], v[146:147] op_sel_hi:[1,0]
	v_cvt_pk_bf16_f32 v142, v144, v145
	v_cvt_pk_bf16_f32 v143, v172, v173
	v_cvt_pk_bf16_f32 v144, v176, v177
	v_cvt_pk_bf16_f32 v145, v174, v175
	v_cvt_pk_bf16_f32 v146, v180, v181
	v_cvt_pk_bf16_f32 v147, v178, v179
	v_cvt_pk_bf16_f32 v148, v184, v185
	v_cvt_pk_bf16_f32 v149, v182, v183
	s_nop 0
	v_cvt_pk_bf16_f32 v150, v188, v189
	v_cvt_pk_bf16_f32 v151, v186, v187
	global_store_dwordx4 v[160:161], v[136:139], off
	global_store_dwordx4 v[160:161], v[140:143], off offset:16
	global_store_dwordx4 v[162:163], v[144:147], off
	global_store_dwordx4 v[162:163], v[148:151], off offset:16
	s_waitcnt vmcnt(10)
	v_pk_mul_f32 v[138:139], v[102:103], v[134:135] op_sel_hi:[1,0]
	v_pk_mul_f32 v[136:137], v[100:101], v[134:135] op_sel_hi:[1,0]
	v_pk_mul_f32 v[140:141], v[98:99], v[134:135] op_sel_hi:[1,0]
	v_cvt_pk_bf16_f32 v136, v136, v137
	v_cvt_pk_bf16_f32 v137, v138, v139
	v_pk_mul_f32 v[142:143], v[96:97], v[134:135] op_sel_hi:[1,0]
	v_cvt_pk_bf16_f32 v139, v140, v141
	v_lshlrev_b64 v[140:141], 13, v[152:153]
	v_lshl_add_u64 v[140:141], v[154:155], 0, v[140:141]
	v_cvt_pk_bf16_f32 v138, v142, v143
	global_store_dwordx4 v[140:141], v[136:139], off
	v_pk_mul_f32 v[142:143], v[66:67], v[134:135] op_sel_hi:[1,0]
	v_pk_mul_f32 v[144:145], v[64:65], v[134:135] op_sel_hi:[1,0]
	v_pk_mul_f32 v[136:137], v[70:71], v[134:135] op_sel_hi:[1,0]
	v_pk_mul_f32 v[138:139], v[68:69], v[134:135] op_sel_hi:[1,0]
	v_cvt_pk_bf16_f32 v135, v136, v137
	v_cvt_pk_bf16_f32 v136, v144, v145
	v_cvt_pk_bf16_f32 v137, v142, v143
	s_waitcnt vmcnt(10)
	v_pk_mul_f32 v[142:143], v[24:25], v[156:157] op_sel_hi:[1,0]
	v_cvt_pk_bf16_f32 v134, v138, v139
	global_store_dwordx4 v[140:141], v[134:137], off offset:16
	v_pk_mul_f32 v[138:139], v[58:59], v[156:157] op_sel_hi:[1,0]
	v_pk_mul_f32 v[140:141], v[56:57], v[156:157] op_sel_hi:[1,0]
	v_pk_mul_f32 v[136:137], v[62:63], v[156:157] op_sel_hi:[1,0]
	v_pk_mul_f32 v[134:135], v[60:61], v[156:157] op_sel_hi:[1,0]
	s_nop 0
	v_cvt_pk_bf16_f32 v134, v134, v135
	v_cvt_pk_bf16_f32 v135, v136, v137
	v_cvt_pk_bf16_f32 v137, v138, v139
	v_lshl_add_u64 v[138:139], v[128:129], 0, s[4:5]
	s_mov_b32 s4, 0x100000
	v_cvt_pk_bf16_f32 v136, v140, v141
	v_add_co_u32_e32 v140, vcc, s4, v128
	s_mov_b64 s[4:5], 0x120000
	s_nop 0
	v_addc_co_u32_e32 v141, vcc, 0, v129, vcc
	global_store_dwordx4 v[140:141], v[134:137], off
	v_pk_mul_f32 v[140:141], v[26:27], v[156:157] op_sel_hi:[1,0]
	s_nop 0
	v_pk_mul_f32 v[136:137], v[30:31], v[156:157] op_sel_hi:[1,0]
	v_pk_mul_f32 v[134:135], v[28:29], v[156:157] op_sel_hi:[1,0]
	s_nop 0
	v_cvt_pk_bf16_f32 v134, v134, v135
	v_cvt_pk_bf16_f32 v135, v136, v137
	v_cvt_pk_bf16_f32 v136, v142, v143
	v_cvt_pk_bf16_f32 v137, v140, v141
	global_store_dwordx4 v[138:139], v[134:137], off offset:16
	s_waitcnt vmcnt(12)
	v_pk_mul_f32 v[138:139], v[50:51], v[158:159] op_sel_hi:[1,0]
	v_pk_mul_f32 v[140:141], v[48:49], v[158:159] op_sel_hi:[1,0]
	v_pk_mul_f32 v[136:137], v[54:55], v[158:159] op_sel_hi:[1,0]
	v_pk_mul_f32 v[134:135], v[52:53], v[158:159] op_sel_hi:[1,0]
	v_pk_mul_f32 v[142:143], v[16:17], v[158:159] op_sel_hi:[1,0]
	v_cvt_pk_bf16_f32 v134, v134, v135
	v_cvt_pk_bf16_f32 v135, v136, v137
	v_cvt_pk_bf16_f32 v137, v138, v139
	v_lshl_add_u64 v[138:139], v[128:129], 0, s[4:5]
	s_mov_b32 s4, 0x120000
	v_cvt_pk_bf16_f32 v136, v140, v141
	v_add_co_u32_e32 v140, vcc, s4, v128
	s_mov_b64 s[4:5], 0x140000
	s_nop 0
	v_addc_co_u32_e32 v141, vcc, 0, v129, vcc
	global_store_dwordx4 v[140:141], v[134:137], off
	v_pk_mul_f32 v[140:141], v[18:19], v[158:159] op_sel_hi:[1,0]
	s_nop 0
	v_pk_mul_f32 v[136:137], v[22:23], v[158:159] op_sel_hi:[1,0]
	v_pk_mul_f32 v[134:135], v[20:21], v[158:159] op_sel_hi:[1,0]
	s_nop 0
	v_cvt_pk_bf16_f32 v134, v134, v135
	v_cvt_pk_bf16_f32 v135, v136, v137
	v_cvt_pk_bf16_f32 v136, v142, v143
	v_cvt_pk_bf16_f32 v137, v140, v141
	global_store_dwordx4 v[138:139], v[134:137], off offset:16
	s_waitcnt vmcnt(13)
	v_pk_mul_f32 v[138:139], v[42:43], v[132:133] op_sel_hi:[1,0]
	v_pk_mul_f32 v[140:141], v[40:41], v[132:133] op_sel_hi:[1,0]
	v_pk_mul_f32 v[136:137], v[46:47], v[132:133] op_sel_hi:[1,0]
	v_pk_mul_f32 v[134:135], v[44:45], v[132:133] op_sel_hi:[1,0]
	v_pk_mul_f32 v[142:143], v[8:9], v[132:133] op_sel_hi:[1,0]
	v_cvt_pk_bf16_f32 v134, v134, v135
	v_cvt_pk_bf16_f32 v135, v136, v137
	v_cvt_pk_bf16_f32 v137, v138, v139
	v_lshl_add_u64 v[138:139], v[128:129], 0, s[4:5]
	s_mov_b32 s4, 0x140000
	v_cvt_pk_bf16_f32 v136, v140, v141
	v_add_co_u32_e32 v140, vcc, s4, v128
	s_mov_b64 s[4:5], 0x160000
	s_nop 0
	v_addc_co_u32_e32 v141, vcc, 0, v129, vcc
	global_store_dwordx4 v[140:141], v[134:137], off
	v_pk_mul_f32 v[140:141], v[10:11], v[132:133] op_sel_hi:[1,0]
	s_nop 0
	v_pk_mul_f32 v[134:135], v[14:15], v[132:133] op_sel_hi:[1,0]
	v_pk_mul_f32 v[136:137], v[12:13], v[132:133] op_sel_hi:[1,0]
	v_cvt_pk_bf16_f32 v133, v134, v135
	v_cvt_pk_bf16_f32 v134, v142, v143
	v_cvt_pk_bf16_f32 v135, v140, v141
	s_nop 0
	v_cvt_pk_bf16_f32 v132, v136, v137
	global_store_dwordx4 v[138:139], v[132:135], off offset:16
	s_waitcnt vmcnt(14)
	v_pk_mul_f32 v[136:137], v[34:35], v[130:131] op_sel_hi:[1,0]
	v_pk_mul_f32 v[138:139], v[32:33], v[130:131] op_sel_hi:[1,0]
	v_pk_mul_f32 v[134:135], v[38:39], v[130:131] op_sel_hi:[1,0]
	v_pk_mul_f32 v[132:133], v[36:37], v[130:131] op_sel_hi:[1,0]
	s_nop 0
	v_cvt_pk_bf16_f32 v132, v132, v133
	v_cvt_pk_bf16_f32 v133, v134, v135
	v_cvt_pk_bf16_f32 v135, v136, v137
	v_lshl_add_u64 v[136:137], v[128:129], 0, s[4:5]
	s_mov_b32 s4, 0x160000
	v_add_co_u32_e32 v128, vcc, s4, v128
	v_cvt_pk_bf16_f32 v134, v138, v139
	s_nop 1
	v_addc_co_u32_e32 v129, vcc, 0, v129, vcc
	global_store_dwordx4 v[128:129], v[132:135], off
	v_pk_mul_f32 v[128:129], v[4:5], v[130:131] op_sel_hi:[1,0]
	s_and_b64 vcc, exec, s[0:1]
	v_pk_mul_f32 v[132:133], v[6:7], v[130:131] op_sel_hi:[1,0]
	v_pk_mul_f32 v[134:135], v[2:3], v[130:131] op_sel_hi:[1,0]
	v_pk_mul_f32 v[130:131], v[0:1], v[130:131] op_sel_hi:[1,0]
	s_mov_b64 s[0:1], -1
	v_cvt_pk_bf16_f32 v128, v128, v129
	v_cvt_pk_bf16_f32 v129, v132, v133
	v_cvt_pk_bf16_f32 v130, v130, v131
	v_cvt_pk_bf16_f32 v131, v134, v135
	global_store_dwordx4 v[136:137], v[128:131], off offset:16
	s_cbranch_vccnz .LBB0_329
	v_readlane_b32 s0, v249, 5
	v_readlane_b32 s1, v249, 6
	s_andn2_b64 vcc, exec, s[0:1]
	s_cbranch_vccnz .LBB0_328
	s_barrier
	s_branch .LBB0_328
	s_nop 0
